# baseline (speedup 1.0000x reference)
.Lmy_conv_skip4:
	s_add_u32 s4, s10, s2
	v_mov_b32_e32 v10, 0
	s_addc_u32 s5, s11, 0
	v_lshlrev_b32_e32 v2, 4, v1
	v_mov_b32_e32 v3, v10
	v_lshl_add_u64 v[130:131], s[4:5], 0, v[2:3]
	v_and_b32_e32 v2, 8, v0
	v_lshlrev_b32_e32 v2, 4, v2
	s_mul_i32 s2, s23, 0xc0
	s_mov_b32 s3, 0
	v_sub_co_u32_e32 v132, vcc, v130, v2
	s_ashr_i32 s5, s2, 31
	s_mov_b32 s4, s2
	v_subbrev_co_u32_e32 v133, vcc, 0, v131, vcc
	v_lshl_add_u64 v[12:13], s[2:3], 4, v[130:131]
	s_lshl_b64 s[4:5], s[4:5], 4
	v_lshl_add_u64 v[14:15], v[130:131], 0, s[4:5]
	global_load_dwordx4 v[2:5], v[12:13], off
	global_load_dwordx4 v[6:9], v[14:15], off offset:1024
	v_lshl_add_u64 v[12:13], v[132:133], 0, s[4:5]
	s_add_i32 s4, s2, 0x600
	s_mov_b32 s5, s3
	v_lshl_add_u64 v[14:15], s[4:5], 4, v[130:131]
	s_ashr_i32 s5, s4, 31
	s_lshl_b64 s[4:5], s[4:5], 4
	global_load_dwordx4 v[98:101], v[12:13], off offset:2048
	global_load_dwordx4 v[86:89], v[14:15], off
	v_lshl_add_u64 v[12:13], v[130:131], 0, s[4:5]
	v_lshl_add_u64 v[14:15], v[132:133], 0, s[4:5]
	s_add_i32 s4, s2, 0xc00
	s_mov_b32 s5, s3
	global_load_dwordx4 v[90:93], v[12:13], off offset:1024
	global_load_dwordx4 v[94:97], v[14:15], off offset:2048
	v_lshl_add_u64 v[12:13], s[4:5], 4, v[130:131]
	s_ashr_i32 s5, s4, 31
	s_lshl_b64 s[4:5], s[4:5], 4
	v_lshl_add_u64 v[14:15], v[130:131], 0, s[4:5]
	global_load_dwordx4 v[74:77], v[12:13], off
	global_load_dwordx4 v[78:81], v[14:15], off offset:1024
	v_lshl_add_u64 v[12:13], v[132:133], 0, s[4:5]
	s_add_i32 s4, s2, 0x1200
	s_mov_b32 s5, s3
	v_lshl_add_u64 v[14:15], s[4:5], 4, v[130:131]
	s_ashr_i32 s5, s4, 31
	s_lshl_b64 s[4:5], s[4:5], 4
	global_load_dwordx4 v[82:85], v[12:13], off offset:2048
	global_load_dwordx4 v[62:65], v[14:15], off
	v_lshl_add_u64 v[12:13], v[130:131], 0, s[4:5]
	s_addk_i32 s2, 0x1800
	v_lshl_add_u64 v[14:15], v[132:133], 0, s[4:5]
	global_load_dwordx4 v[66:69], v[12:13], off offset:1024
	global_load_dwordx4 v[70:73], v[14:15], off offset:2048
	v_lshl_add_u64 v[12:13], s[2:3], 4, v[130:131]
	s_ashr_i32 s3, s2, 31
	s_lshl_b64 s[2:3], s[2:3], 4
	v_lshl_add_u64 v[14:15], v[130:131], 0, s[2:3]
	global_load_dwordx4 v[50:53], v[12:13], off
	global_load_dwordx4 v[54:57], v[14:15], off offset:1024
	v_lshl_add_u64 v[12:13], v[132:133], 0, s[2:3]
	global_load_dwordx4 v[58:61], v[12:13], off offset:2048
	s_load_dwordx8 s[4:11], s[0:1], 0x10
	s_load_dwordx2 s[12:13], s[0:1], 0x30
	v_lshl_add_u32 v118, v1, 3, s23
	s_mov_b32 s26, 0xcccd
	v_mul_u32_u24_e32 v119, s26, v118
	v_lshrrev_b32_e32 v119, 18, v119
	v_mul_u32_u24_e32 v120, 5, v119
	v_sub_u32_e32 v120, v118, v120
	v_mul_u32_u24_e32 v121, 57, v119
	v_lshrrev_b32_e32 v121, 9, v121
	v_mul_u32_u24_e32 v122, 9, v121
	v_sub_u32_e32 v122, v119, v122
	v_mul_u32_u24_e32 v123, 11, v122
	v_lshrrev_b32_e32 v123, 5, v123
	v_mul_u32_u24_e32 v124, 3, v123
	v_sub_u32_e32 v124, v122, v124
	v_mul_u32_u24_e32 v125, 36, v121
	v_mad_u32_u24 v125, v123, 6, v125
	v_add_u32_e32 v125, v125, v124
	s_movk_i32 s26, 0x160
	v_mul_u32_u24_e32 v125, s26, v125
	v_lshl_add_u32 v125, v120, 6, v125
	s_nop 1
	v_readlane_b32 s48, v125, 0
	v_readlane_b32 s49, v125, 1
	v_readlane_b32 s50, v125, 2
	v_readlane_b32 s51, v125, 3
	v_readlane_b32 s52, v125, 4
	v_readlane_b32 s53, v125, 5
	v_readlane_b32 s54, v125, 6
	v_readlane_b32 s55, v125, 7
	v_readlane_b32 s56, v125, 8
	v_readlane_b32 s57, v125, 9
	v_readlane_b32 s58, v125, 10
	v_readlane_b32 s59, v125, 11
	v_readlane_b32 s60, v125, 12
	v_readlane_b32 s61, v125, 13
	v_readlane_b32 s62, v125, 14
	v_readlane_b32 s63, v125, 15
	v_readlane_b32 s64, v125, 16
	s_mul_i32 s26, s23, 0x840
	v_add_u32_e32 v20, s26, v20
	v_add_u32_e32 v22, s26, v22
	s_waitcnt vmcnt(15)
	ds_write_b128 v20, v[24:27]
	ds_write_b128 v20, v[32:35] offset:16896
	ds_write_b128 v20, v[40:43] offset:33792
	ds_write_b128 v20, v[102:105] offset:50688
	s_mov_b64 exec, s[18:19]
	ds_write_b128 v22, v[28:31]
	ds_write_b128 v22, v[36:39] offset:16896
	ds_write_b128 v22, v[44:47] offset:33792
	ds_write_b128 v22, v[106:109] offset:50688
	s_mov_b64 exec, -1
	s_cmp_gt_u32 s23, 3
	s_cbranch_scc1 .Lmy_conv_nor5
	v_add_u32_e32 v20, 0x10800, v20
	v_add_u32_e32 v22, 0x10800, v22
	ds_write_b128 v20, v[110:113]
	s_mov_b64 exec, s[18:19]
	ds_write_b128 v22, v[114:117]
	s_mov_b64 exec, -1
.Lmy_conv_nor5:
	v_and_b32_e32 v135, 15, v0
	s_mul_i32 s25, s25, 40
	v_add_lshl_u32 v10, v135, s25, 2
	v_or_b32_e32 v11, 32, v135
	s_waitcnt lgkmcnt(0)
	global_load_dword v14, v10, s[12:13]
	global_load_dword v140, v10, s[4:5]
	global_load_dword v141, v10, s[10:11]
	global_load_dword v134, v10, s[8:9]
	global_load_dword v138, v10, s[6:7] offset:64
	global_load_dword v139, v10, s[4:5] offset:64
	global_load_dword v15, v10, s[12:13] offset:64
	v_cmp_gt_u32_e32 vcc, 40, v11
	s_min_u32 s2, s23, 0x5e
	s_mulk_i32 s2, 0xc00
	v_cndmask_b32_e32 v11, 0, v11, vcc
	v_add_lshl_u32 v11, v11, s25, 2
	global_load_dword v142, v11, s[4:5]
	global_load_dword v143, v11, s[10:11]
	global_load_dword v136, v11, s[8:9]
	global_load_dword v16, v11, s[12:13]
	global_load_dword v146, v10, s[6:7]
	global_load_dword v144, v11, s[6:7]
	s_mov_b32 s19, 0
	s_add_i32 s18, s2, 0x1e000
	global_load_dword v145, v10, s[10:11] offset:64
	global_load_dword v137, v10, s[8:9] offset:64
	v_lshl_add_u64 v[10:11], v[130:131], 0, s[18:19]
	v_lshl_add_u64 v[12:13], v[132:133], 0, s[18:19]
	s_barrier
	global_load_dwordx4 v[102:105], v[10:11], off
	global_load_dwordx4 v[106:109], v[10:11], off offset:1024
	global_load_dwordx4 v[110:113], v[12:13], off offset:2048
	v_and_b32_e32 v11, 3, v0
	v_bfe_u32 v12, v0, 2, 2
	s_mov_b32 s4, 0xf800000
	v_mad_u32_u24 v11, v11, 6, v12
	v_and_b32_e32 v10, 48, v0
	s_movk_i32 s18, 0x160
	v_mad_u32_u24 v150, v11, s18, v10
	s_waitcnt vmcnt(17)
	v_add_f32_e32 v12, 0x3727c5ac, v14
	v_mul_f32_e32 v14, 0x4f800000, v12
	v_cmp_gt_f32_e32 vcc, s4, v12
	s_waitcnt vmcnt(11)
	v_add_f32_e32 v13, 0x3727c5ac, v15
	v_mul_f32_e32 v15, 0x4f800000, v13
	v_cndmask_b32_e32 v147, v12, v14, vcc
	v_cmp_gt_f32_e64 s[2:3], s4, v13
	s_waitcnt vmcnt(7)
	v_add_f32_e32 v12, 0x3727c5ac, v16
	v_cmp_gt_f32_e64 s[4:5], s4, v12
	v_cndmask_b32_e64 v148, v13, v15, s[2:3]
	v_mul_f32_e32 v13, 0x4f800000, v12
	v_sqrt_f32_e32 v154, v147
	v_cndmask_b32_e64 v149, v12, v13, s[4:5]
	v_sqrt_f32_e32 v155, v148
	v_sqrt_f32_e32 v156, v149
	v_add_u32_e32 v157, -1, v154
	v_add_u32_e32 v151, 1, v154
	v_add_u32_e32 v158, -1, v155
	v_add_u32_e32 v152, 1, v155
	v_fma_f32 v12, -v157, v154, v147
	v_fma_f32 v13, -v151, v154, v147
	v_add_u32_e32 v159, -1, v156
	v_add_u32_e32 v153, 1, v156
	v_fma_f32 v14, -v158, v155, v148
	v_fma_f32 v15, -v152, v155, v148
	v_cmp_ge_f32_e64 s[12:13], 0, v12
	v_cmp_lt_f32_e64 s[6:7], 0, v13
	v_fma_f32 v12, -v159, v156, v149
	v_fma_f32 v13, -v153, v156, v149
	v_cmp_ge_f32_e64 s[14:15], 0, v14
	v_cmp_lt_f32_e64 s[8:9], 0, v15
	v_cmp_ge_f32_e64 s[16:17], 0, v12
	v_cmp_lt_f32_e64 s[10:11], 0, v13
	s_cmpk_gt_u32 s24, 0x21bf
	s_cbranch_scc1 .LBB0_24
	v_add_u32_e32 v14, s48, v150
	ds_read_b128 v[10:13], v14
	ds_read_b128 v[114:117], v14 offset:38016
	s_waitcnt lgkmcnt(1)
	v_mfma_f32_16x16x32_f16 v[46:49], v[10:13], v[2:5], 0
	v_mfma_f32_16x16x32_f16 v[42:45], v[10:13], v[6:9], 0
	v_mfma_f32_16x16x32_f16 v[34:37], v[10:13], v[98:101], 0
	ds_read_b128 v[10:13], v14 offset:12672
	ds_read_b128 v[14:17], v14 offset:25344
	s_waitcnt lgkmcnt(1)
	v_mfma_f32_16x16x32_f16 v[38:41], v[10:13], v[2:5], 0
	v_mfma_f32_16x16x32_f16 v[30:33], v[10:13], v[6:9], 0
	v_mfma_f32_16x16x32_f16 v[26:29], v[10:13], v[98:101], 0
	s_waitcnt lgkmcnt(0)
	v_mfma_f32_16x16x32_f16 v[22:25], v[14:17], v[2:5], 0
	v_mfma_f32_16x16x32_f16 v[18:21], v[14:17], v[6:9], 0
	v_mfma_f32_16x16x32_f16 v[14:17], v[14:17], v[98:101], 0
	v_mfma_f32_16x16x32_f16 v[10:13], v[114:117], v[2:5], 0
	v_mfma_f32_16x16x32_f16 v[6:9], v[114:117], v[6:9], 0
	v_mfma_f32_16x16x32_f16 v[2:5], v[114:117], v[98:101], 0
	s_branch .LBB0_25

.LBB0_25:
	s_min_u32 s18, s23, 0x56
	s_mulk_i32 s18, 0xc00
	s_add_i32 s18, s18, 0x24000
	v_lshl_add_u64 v[114:115], v[130:131], 0, s[18:19]
	v_lshl_add_u64 v[118:119], v[132:133], 0, s[18:19]
	global_load_dwordx4 v[98:101], v[114:115], off
	s_nop 0
	global_load_dwordx4 v[114:117], v[114:115], off offset:1024
	s_nop 0
	global_load_dwordx4 v[118:121], v[118:119], off offset:2048
	s_cmpk_gt_u32 s24, 0x1fbf
	s_cbranch_scc1 .LBB0_27
	v_add_u32_e32 v160, s49, v150
	ds_read_b128 v[122:125], v160
	ds_read_b128 v[126:129], v160 offset:38016
	s_waitcnt lgkmcnt(1)
	v_mfma_f32_16x16x32_f16 v[46:49], v[122:125], v[86:89], v[46:49]
	v_mfma_f32_16x16x32_f16 v[42:45], v[122:125], v[90:93], v[42:45]
	v_mfma_f32_16x16x32_f16 v[34:37], v[122:125], v[94:97], v[34:37]
	ds_read_b128 v[122:125], v160 offset:12672
	ds_read_b128 v[160:163], v160 offset:25344
	s_waitcnt lgkmcnt(1)
	v_mfma_f32_16x16x32_f16 v[38:41], v[122:125], v[86:89], v[38:41]
	v_mfma_f32_16x16x32_f16 v[30:33], v[122:125], v[90:93], v[30:33]
	v_mfma_f32_16x16x32_f16 v[26:29], v[122:125], v[94:97], v[26:29]
	s_waitcnt lgkmcnt(0)
	v_mfma_f32_16x16x32_f16 v[22:25], v[160:163], v[86:89], v[22:25]
	v_mfma_f32_16x16x32_f16 v[18:21], v[160:163], v[90:93], v[18:21]
	v_mfma_f32_16x16x32_f16 v[14:17], v[160:163], v[94:97], v[14:17]
	v_mfma_f32_16x16x32_f16 v[10:13], v[126:129], v[86:89], v[10:13]
	v_mfma_f32_16x16x32_f16 v[6:9], v[126:129], v[90:93], v[6:9]
	v_mfma_f32_16x16x32_f16 v[2:5], v[126:129], v[94:97], v[2:5]
.LBB0_27:
	s_min_u32 s18, s23, 0x4e
	s_mulk_i32 s18, 0xc00
	s_add_i32 s18, s18, 0x2a000
	s_mov_b32 s19, 0
	v_lshl_add_u64 v[90:91], v[130:131], 0, s[18:19]
	v_lshl_add_u64 v[94:95], v[132:133], 0, s[18:19]
	global_load_dwordx4 v[86:89], v[90:91], off
	s_nop 0
	global_load_dwordx4 v[90:93], v[90:91], off offset:1024
	s_nop 0
	global_load_dwordx4 v[122:125], v[94:95], off offset:2048
	s_cmpk_gt_u32 s24, 0x1dbf
	s_cbranch_scc1 .LBB0_29
	v_add_u32_e32 v160, s50, v150
	ds_read_b128 v[94:97], v160
	ds_read_b128 v[126:129], v160 offset:38016
	s_waitcnt lgkmcnt(1)
	v_mfma_f32_16x16x32_f16 v[46:49], v[94:97], v[74:77], v[46:49]
	v_mfma_f32_16x16x32_f16 v[42:45], v[94:97], v[78:81], v[42:45]
	v_mfma_f32_16x16x32_f16 v[34:37], v[94:97], v[82:85], v[34:37]
	ds_read_b128 v[94:97], v160 offset:12672
	ds_read_b128 v[160:163], v160 offset:25344
	s_waitcnt lgkmcnt(1)
	v_mfma_f32_16x16x32_f16 v[38:41], v[94:97], v[74:77], v[38:41]
	v_mfma_f32_16x16x32_f16 v[30:33], v[94:97], v[78:81], v[30:33]
	v_mfma_f32_16x16x32_f16 v[26:29], v[94:97], v[82:85], v[26:29]
	s_waitcnt lgkmcnt(0)
	v_mfma_f32_16x16x32_f16 v[22:25], v[160:163], v[74:77], v[22:25]
	v_mfma_f32_16x16x32_f16 v[18:21], v[160:163], v[78:81], v[18:21]
	v_mfma_f32_16x16x32_f16 v[14:17], v[160:163], v[82:85], v[14:17]
	v_mfma_f32_16x16x32_f16 v[10:13], v[126:129], v[74:77], v[10:13]
	v_mfma_f32_16x16x32_f16 v[6:9], v[126:129], v[78:81], v[6:9]
	v_mfma_f32_16x16x32_f16 v[2:5], v[126:129], v[82:85], v[2:5]
.LBB0_29:
	s_min_u32 s18, s23, 0x46
	s_mulk_i32 s18, 0xc00
	s_add_i32 s18, s18, 0x30000
	v_lshl_add_u64 v[78:79], v[130:131], 0, s[18:19]
	v_lshl_add_u64 v[82:83], v[132:133], 0, s[18:19]
	global_load_dwordx4 v[74:77], v[78:79], off
	s_nop 0
	global_load_dwordx4 v[78:81], v[78:79], off offset:1024
	s_nop 0
	global_load_dwordx4 v[82:85], v[82:83], off offset:2048
	s_cmpk_gt_u32 s24, 0x1bbf
	s_cbranch_scc1 .LBB0_31
	v_add_u32_e32 v160, s51, v150
	ds_read_b128 v[94:97], v160
	ds_read_b128 v[126:129], v160 offset:38016
	s_waitcnt lgkmcnt(1)
	v_mfma_f32_16x16x32_f16 v[46:49], v[94:97], v[62:65], v[46:49]
	v_mfma_f32_16x16x32_f16 v[42:45], v[94:97], v[66:69], v[42:45]
	v_mfma_f32_16x16x32_f16 v[34:37], v[94:97], v[70:73], v[34:37]
	ds_read_b128 v[94:97], v160 offset:12672
	ds_read_b128 v[160:163], v160 offset:25344
	s_waitcnt lgkmcnt(1)
	v_mfma_f32_16x16x32_f16 v[38:41], v[94:97], v[62:65], v[38:41]
	v_mfma_f32_16x16x32_f16 v[30:33], v[94:97], v[66:69], v[30:33]
	v_mfma_f32_16x16x32_f16 v[26:29], v[94:97], v[70:73], v[26:29]
	s_waitcnt lgkmcnt(0)
	v_mfma_f32_16x16x32_f16 v[22:25], v[160:163], v[62:65], v[22:25]
	v_mfma_f32_16x16x32_f16 v[18:21], v[160:163], v[66:69], v[18:21]
	v_mfma_f32_16x16x32_f16 v[14:17], v[160:163], v[70:73], v[14:17]
	v_mfma_f32_16x16x32_f16 v[10:13], v[126:129], v[62:65], v[10:13]
	v_mfma_f32_16x16x32_f16 v[6:9], v[126:129], v[66:69], v[6:9]
	v_mfma_f32_16x16x32_f16 v[2:5], v[126:129], v[70:73], v[2:5]
.LBB0_31:
	s_min_u32 s18, s23, 62
	s_mulk_i32 s18, 0xc00
	s_add_i32 s18, s18, 0x36000
	s_mov_b32 s19, 0
	v_lshl_add_u64 v[66:67], v[130:131], 0, s[18:19]
	v_lshl_add_u64 v[70:71], v[132:133], 0, s[18:19]
	global_load_dwordx4 v[62:65], v[66:67], off
	s_nop 0
	global_load_dwordx4 v[66:69], v[66:67], off offset:1024
	s_nop 0
	global_load_dwordx4 v[126:129], v[70:71], off offset:2048
	s_cmpk_gt_u32 s24, 0x19bf
	s_cbranch_scc1 .LBB0_33
	v_add_u32_e32 v160, s52, v150
	ds_read_b128 v[70:73], v160
	ds_read_b128 v[94:97], v160 offset:38016
	s_waitcnt lgkmcnt(1)
	v_mfma_f32_16x16x32_f16 v[46:49], v[70:73], v[50:53], v[46:49]
	v_mfma_f32_16x16x32_f16 v[42:45], v[70:73], v[54:57], v[42:45]
	v_mfma_f32_16x16x32_f16 v[34:37], v[70:73], v[58:61], v[34:37]
	ds_read_b128 v[70:73], v160 offset:12672
	ds_read_b128 v[160:163], v160 offset:25344
	s_waitcnt lgkmcnt(1)
	v_mfma_f32_16x16x32_f16 v[38:41], v[70:73], v[50:53], v[38:41]
	v_mfma_f32_16x16x32_f16 v[30:33], v[70:73], v[54:57], v[30:33]
	v_mfma_f32_16x16x32_f16 v[26:29], v[70:73], v[58:61], v[26:29]
	s_waitcnt lgkmcnt(0)
	v_mfma_f32_16x16x32_f16 v[22:25], v[160:163], v[50:53], v[22:25]
	v_mfma_f32_16x16x32_f16 v[18:21], v[160:163], v[54:57], v[18:21]
	v_mfma_f32_16x16x32_f16 v[14:17], v[160:163], v[58:61], v[14:17]
	v_mfma_f32_16x16x32_f16 v[10:13], v[94:97], v[50:53], v[10:13]
	v_mfma_f32_16x16x32_f16 v[6:9], v[94:97], v[54:57], v[6:9]
	v_mfma_f32_16x16x32_f16 v[2:5], v[94:97], v[58:61], v[2:5]
.LBB0_33:
	s_min_u32 s18, s23, 54
	s_mulk_i32 s18, 0xc00
	s_add_i32 s18, s18, 0x3c000
	v_lshl_add_u64 v[54:55], v[130:131], 0, s[18:19]
	v_lshl_add_u64 v[58:59], v[132:133], 0, s[18:19]
	global_load_dwordx4 v[50:53], v[54:55], off
	s_nop 0
	global_load_dwordx4 v[54:57], v[54:55], off offset:1024
	s_nop 0
	global_load_dwordx4 v[58:61], v[58:59], off offset:2048
	s_cmpk_gt_u32 s24, 0x17bf
	s_cbranch_scc1 .LBB0_35
	v_add_u32_e32 v160, s53, v150
	ds_read_b128 v[70:73], v160
	ds_read_b128 v[94:97], v160 offset:38016
	s_waitcnt vmcnt(17) lgkmcnt(1)
	v_mfma_f32_16x16x32_f16 v[46:49], v[70:73], v[102:105], v[46:49]
	s_waitcnt vmcnt(16)
	v_mfma_f32_16x16x32_f16 v[42:45], v[70:73], v[106:109], v[42:45]
	s_waitcnt vmcnt(15)
	v_mfma_f32_16x16x32_f16 v[34:37], v[70:73], v[110:113], v[34:37]
	ds_read_b128 v[70:73], v160 offset:12672
	ds_read_b128 v[160:163], v160 offset:25344
	s_waitcnt lgkmcnt(1)
	v_mfma_f32_16x16x32_f16 v[38:41], v[70:73], v[102:105], v[38:41]
	v_mfma_f32_16x16x32_f16 v[30:33], v[70:73], v[106:109], v[30:33]
	v_mfma_f32_16x16x32_f16 v[26:29], v[70:73], v[110:113], v[26:29]
	s_waitcnt lgkmcnt(0)
	v_mfma_f32_16x16x32_f16 v[22:25], v[160:163], v[102:105], v[22:25]
	v_mfma_f32_16x16x32_f16 v[18:21], v[160:163], v[106:109], v[18:21]
	v_mfma_f32_16x16x32_f16 v[14:17], v[160:163], v[110:113], v[14:17]
	v_mfma_f32_16x16x32_f16 v[10:13], v[94:97], v[102:105], v[10:13]
	v_mfma_f32_16x16x32_f16 v[6:9], v[94:97], v[106:109], v[6:9]
	v_mfma_f32_16x16x32_f16 v[2:5], v[94:97], v[110:113], v[2:5]
.LBB0_35:
	s_min_u32 s18, s23, 46
	s_mulk_i32 s18, 0xc00
	s_add_i32 s18, s18, 0x42000
	s_mov_b32 s19, 0
	v_lshl_add_u64 v[94:95], v[130:131], 0, s[18:19]
	s_waitcnt vmcnt(17)
	v_lshl_add_u64 v[102:103], v[132:133], 0, s[18:19]
	global_load_dwordx4 v[70:73], v[94:95], off
	s_nop 0
	global_load_dwordx4 v[94:97], v[94:95], off offset:1024
	s_nop 0
	global_load_dwordx4 v[102:105], v[102:103], off offset:2048
	s_cmpk_gt_u32 s24, 0x15bf
	s_cbranch_scc1 .LBB0_37
	v_add_u32_e32 v160, s54, v150
	s_waitcnt vmcnt(19)
	ds_read_b128 v[106:109], v160
	s_waitcnt vmcnt(18)
	ds_read_b128 v[110:113], v160 offset:38016
	s_waitcnt vmcnt(17) lgkmcnt(1)
	v_mfma_f32_16x16x32_f16 v[46:49], v[106:109], v[98:101], v[46:49]
	s_waitcnt vmcnt(16)
	v_mfma_f32_16x16x32_f16 v[42:45], v[106:109], v[114:117], v[42:45]
	s_waitcnt vmcnt(15)
	v_mfma_f32_16x16x32_f16 v[34:37], v[106:109], v[118:121], v[34:37]
	ds_read_b128 v[106:109], v160 offset:12672
	ds_read_b128 v[160:163], v160 offset:25344
	s_waitcnt lgkmcnt(1)
	v_mfma_f32_16x16x32_f16 v[38:41], v[106:109], v[98:101], v[38:41]
	v_mfma_f32_16x16x32_f16 v[30:33], v[106:109], v[114:117], v[30:33]
	v_mfma_f32_16x16x32_f16 v[26:29], v[106:109], v[118:121], v[26:29]
	s_waitcnt lgkmcnt(0)
	v_mfma_f32_16x16x32_f16 v[22:25], v[160:163], v[98:101], v[22:25]
	v_mfma_f32_16x16x32_f16 v[18:21], v[160:163], v[114:117], v[18:21]
	v_mfma_f32_16x16x32_f16 v[14:17], v[160:163], v[118:121], v[14:17]
	v_mfma_f32_16x16x32_f16 v[10:13], v[110:113], v[98:101], v[10:13]
	v_mfma_f32_16x16x32_f16 v[6:9], v[110:113], v[114:117], v[6:9]
	v_mfma_f32_16x16x32_f16 v[2:5], v[110:113], v[118:121], v[2:5]
.LBB0_37:
	s_min_u32 s18, s23, 38
	s_mulk_i32 s18, 0xc00
	s_add_i32 s18, s18, 0x48000
	s_waitcnt vmcnt(19)
	v_lshl_add_u64 v[106:107], v[130:131], 0, s[18:19]
	s_waitcnt vmcnt(18)
	v_lshl_add_u64 v[110:111], v[132:133], 0, s[18:19]
	global_load_dwordx4 v[98:101], v[106:107], off
	s_nop 0
	global_load_dwordx4 v[106:109], v[106:107], off offset:1024
	s_nop 0
	global_load_dwordx4 v[110:113], v[110:111], off offset:2048
	s_cmpk_gt_u32 s24, 0x13bf
	s_cbranch_scc1 .LBB0_39
	v_add_u32_e32 v160, s55, v150
	s_waitcnt vmcnt(19)
	ds_read_b128 v[114:117], v160
	s_waitcnt vmcnt(18)
	ds_read_b128 v[118:121], v160 offset:38016
	s_waitcnt vmcnt(17) lgkmcnt(1)
	v_mfma_f32_16x16x32_f16 v[46:49], v[114:117], v[86:89], v[46:49]
	s_waitcnt vmcnt(16)
	v_mfma_f32_16x16x32_f16 v[42:45], v[114:117], v[90:93], v[42:45]
	s_waitcnt vmcnt(15)
	v_mfma_f32_16x16x32_f16 v[34:37], v[114:117], v[122:125], v[34:37]
	ds_read_b128 v[114:117], v160 offset:12672
	ds_read_b128 v[160:163], v160 offset:25344
	s_waitcnt lgkmcnt(1)
	v_mfma_f32_16x16x32_f16 v[38:41], v[114:117], v[86:89], v[38:41]
	v_mfma_f32_16x16x32_f16 v[30:33], v[114:117], v[90:93], v[30:33]
	v_mfma_f32_16x16x32_f16 v[26:29], v[114:117], v[122:125], v[26:29]
	s_waitcnt lgkmcnt(0)
	v_mfma_f32_16x16x32_f16 v[22:25], v[160:163], v[86:89], v[22:25]
	v_mfma_f32_16x16x32_f16 v[18:21], v[160:163], v[90:93], v[18:21]
	v_mfma_f32_16x16x32_f16 v[14:17], v[160:163], v[122:125], v[14:17]
	v_mfma_f32_16x16x32_f16 v[10:13], v[118:121], v[86:89], v[10:13]
	v_mfma_f32_16x16x32_f16 v[6:9], v[118:121], v[90:93], v[6:9]
	v_mfma_f32_16x16x32_f16 v[2:5], v[118:121], v[122:125], v[2:5]
.LBB0_39:
	s_min_u32 s18, s23, 30
	s_mulk_i32 s18, 0xc00
	s_add_i32 s18, s18, 0x4e000
	s_mov_b32 s19, 0
	s_waitcnt vmcnt(16)
	v_lshl_add_u64 v[90:91], v[130:131], 0, s[18:19]
	v_lshl_add_u64 v[114:115], v[132:133], 0, s[18:19]
	global_load_dwordx4 v[86:89], v[90:91], off
	s_nop 0
	global_load_dwordx4 v[90:93], v[90:91], off offset:1024
	s_nop 0
	global_load_dwordx4 v[114:117], v[114:115], off offset:2048
	s_cmpk_gt_u32 s24, 0x11bf
	s_cbranch_scc1 .LBB0_41
	v_add_u32_e32 v160, s56, v150
	ds_read_b128 v[118:121], v160
	s_waitcnt vmcnt(18)
	ds_read_b128 v[122:125], v160 offset:38016
	s_waitcnt vmcnt(17) lgkmcnt(1)
	v_mfma_f32_16x16x32_f16 v[46:49], v[118:121], v[74:77], v[46:49]
	s_waitcnt vmcnt(16)
	v_mfma_f32_16x16x32_f16 v[42:45], v[118:121], v[78:81], v[42:45]
	s_waitcnt vmcnt(15)
	v_mfma_f32_16x16x32_f16 v[34:37], v[118:121], v[82:85], v[34:37]
	ds_read_b128 v[118:121], v160 offset:12672
	ds_read_b128 v[160:163], v160 offset:25344
	s_waitcnt lgkmcnt(1)
	v_mfma_f32_16x16x32_f16 v[38:41], v[118:121], v[74:77], v[38:41]
	v_mfma_f32_16x16x32_f16 v[30:33], v[118:121], v[78:81], v[30:33]
	v_mfma_f32_16x16x32_f16 v[26:29], v[118:121], v[82:85], v[26:29]
	s_waitcnt lgkmcnt(0)
	v_mfma_f32_16x16x32_f16 v[22:25], v[160:163], v[74:77], v[22:25]
	v_mfma_f32_16x16x32_f16 v[18:21], v[160:163], v[78:81], v[18:21]
	v_mfma_f32_16x16x32_f16 v[14:17], v[160:163], v[82:85], v[14:17]
	v_mfma_f32_16x16x32_f16 v[10:13], v[122:125], v[74:77], v[10:13]
	v_mfma_f32_16x16x32_f16 v[6:9], v[122:125], v[78:81], v[6:9]
	v_mfma_f32_16x16x32_f16 v[2:5], v[122:125], v[82:85], v[2:5]
.LBB0_41:
	s_min_u32 s18, s23, 22
	s_mulk_i32 s18, 0xc00
	s_add_i32 s18, s18, 0x54000
	s_waitcnt vmcnt(16)
	v_lshl_add_u64 v[78:79], v[130:131], 0, s[18:19]
	s_waitcnt vmcnt(15)
	v_lshl_add_u64 v[82:83], v[132:133], 0, s[18:19]
	global_load_dwordx4 v[74:77], v[78:79], off
	s_nop 0
	global_load_dwordx4 v[78:81], v[78:79], off offset:1024
	s_nop 0
	global_load_dwordx4 v[82:85], v[82:83], off offset:2048
	s_cmpk_gt_u32 s24, 0xfbf
	s_cbranch_scc1 .LBB0_43
	v_add_u32_e32 v160, s57, v150
	ds_read_b128 v[118:121], v160
	ds_read_b128 v[122:125], v160 offset:38016
	s_waitcnt vmcnt(17) lgkmcnt(1)
	v_mfma_f32_16x16x32_f16 v[46:49], v[118:121], v[62:65], v[46:49]
	s_waitcnt vmcnt(16)
	v_mfma_f32_16x16x32_f16 v[42:45], v[118:121], v[66:69], v[42:45]
	s_waitcnt vmcnt(15)
	v_mfma_f32_16x16x32_f16 v[34:37], v[118:121], v[126:129], v[34:37]
	ds_read_b128 v[118:121], v160 offset:12672
	ds_read_b128 v[160:163], v160 offset:25344
	s_waitcnt lgkmcnt(1)
	v_mfma_f32_16x16x32_f16 v[38:41], v[118:121], v[62:65], v[38:41]
	v_mfma_f32_16x16x32_f16 v[30:33], v[118:121], v[66:69], v[30:33]
	v_mfma_f32_16x16x32_f16 v[26:29], v[118:121], v[126:129], v[26:29]
	s_waitcnt lgkmcnt(0)
	v_mfma_f32_16x16x32_f16 v[22:25], v[160:163], v[62:65], v[22:25]
	v_mfma_f32_16x16x32_f16 v[18:21], v[160:163], v[66:69], v[18:21]
	v_mfma_f32_16x16x32_f16 v[14:17], v[160:163], v[126:129], v[14:17]
	v_mfma_f32_16x16x32_f16 v[10:13], v[122:125], v[62:65], v[10:13]
	v_mfma_f32_16x16x32_f16 v[6:9], v[122:125], v[66:69], v[6:9]
	v_mfma_f32_16x16x32_f16 v[2:5], v[122:125], v[126:129], v[2:5]
.LBB0_43:
	s_min_u32 s18, s23, 14
	s_mulk_i32 s18, 0xc00
	s_add_i32 s18, s18, 0x5a000
	s_mov_b32 s19, 0
	s_waitcnt vmcnt(16)
	v_lshl_add_u64 v[66:67], v[130:131], 0, s[18:19]
	v_lshl_add_u64 v[118:119], v[132:133], 0, s[18:19]
	global_load_dwordx4 v[62:65], v[66:67], off
	s_nop 0
	global_load_dwordx4 v[66:69], v[66:67], off offset:1024
	s_nop 0
	global_load_dwordx4 v[118:121], v[118:119], off offset:2048
	s_cmpk_gt_u32 s24, 0xdbf
	s_cbranch_scc1 .LBB0_45
	v_add_u32_e32 v160, s58, v150
	ds_read_b128 v[122:125], v160
	s_waitcnt vmcnt(18)
	ds_read_b128 v[126:129], v160 offset:38016
	s_waitcnt vmcnt(17) lgkmcnt(1)
	v_mfma_f32_16x16x32_f16 v[46:49], v[122:125], v[50:53], v[46:49]
	s_waitcnt vmcnt(16)
	v_mfma_f32_16x16x32_f16 v[42:45], v[122:125], v[54:57], v[42:45]
	s_waitcnt vmcnt(15)
	v_mfma_f32_16x16x32_f16 v[34:37], v[122:125], v[58:61], v[34:37]
	ds_read_b128 v[122:125], v160 offset:12672
	ds_read_b128 v[160:163], v160 offset:25344
	s_waitcnt lgkmcnt(1)
	v_mfma_f32_16x16x32_f16 v[38:41], v[122:125], v[50:53], v[38:41]
	v_mfma_f32_16x16x32_f16 v[30:33], v[122:125], v[54:57], v[30:33]
	v_mfma_f32_16x16x32_f16 v[26:29], v[122:125], v[58:61], v[26:29]
	s_waitcnt lgkmcnt(0)
	v_mfma_f32_16x16x32_f16 v[22:25], v[160:163], v[50:53], v[22:25]
	v_mfma_f32_16x16x32_f16 v[18:21], v[160:163], v[54:57], v[18:21]
	v_mfma_f32_16x16x32_f16 v[14:17], v[160:163], v[58:61], v[14:17]
	v_mfma_f32_16x16x32_f16 v[10:13], v[126:129], v[50:53], v[10:13]
	v_mfma_f32_16x16x32_f16 v[6:9], v[126:129], v[54:57], v[6:9]
	v_mfma_f32_16x16x32_f16 v[2:5], v[126:129], v[58:61], v[2:5]
.LBB0_45:
	s_min_u32 s18, s23, 6
	s_mulk_i32 s18, 0xc00
	s_or_b32 s18, s18, 0x60000
	s_waitcnt vmcnt(16)
	v_lshl_add_u64 v[54:55], v[130:131], 0, s[18:19]
	s_waitcnt vmcnt(15)
	v_lshl_add_u64 v[58:59], v[132:133], 0, s[18:19]
	global_load_dwordx4 v[50:53], v[54:55], off
	s_nop 0
	global_load_dwordx4 v[54:57], v[54:55], off offset:1024
	s_nop 0
	global_load_dwordx4 v[58:61], v[58:59], off offset:2048
	s_cmpk_gt_u32 s24, 0xbbf
	s_cbranch_scc1 .LBB0_47
	v_add_u32_e32 v130, s59, v150
	ds_read_b128 v[122:125], v130
	ds_read_b128 v[126:129], v130 offset:38016
	s_waitcnt vmcnt(17) lgkmcnt(1)
	v_mfma_f32_16x16x32_f16 v[46:49], v[122:125], v[70:73], v[46:49]
	s_waitcnt vmcnt(16)
	v_mfma_f32_16x16x32_f16 v[42:45], v[122:125], v[94:97], v[42:45]
	s_waitcnt vmcnt(15)
	v_mfma_f32_16x16x32_f16 v[34:37], v[122:125], v[102:105], v[34:37]
	ds_read_b128 v[122:125], v130 offset:12672
	ds_read_b128 v[130:133], v130 offset:25344
	s_waitcnt lgkmcnt(1)
	v_mfma_f32_16x16x32_f16 v[38:41], v[122:125], v[70:73], v[38:41]
	v_mfma_f32_16x16x32_f16 v[30:33], v[122:125], v[94:97], v[30:33]
	v_mfma_f32_16x16x32_f16 v[26:29], v[122:125], v[102:105], v[26:29]
	s_waitcnt lgkmcnt(0)
	v_mfma_f32_16x16x32_f16 v[22:25], v[130:133], v[70:73], v[22:25]
	v_mfma_f32_16x16x32_f16 v[18:21], v[130:133], v[94:97], v[18:21]
	v_mfma_f32_16x16x32_f16 v[14:17], v[130:133], v[102:105], v[14:17]
	v_mfma_f32_16x16x32_f16 v[10:13], v[126:129], v[70:73], v[10:13]
	v_mfma_f32_16x16x32_f16 v[6:9], v[126:129], v[94:97], v[6:9]
	v_mfma_f32_16x16x32_f16 v[2:5], v[126:129], v[102:105], v[2:5]
.LBB0_47:
	s_waitcnt vmcnt(17)
	v_cndmask_b32_e64 v70, v154, v157, s[12:13]
	v_cndmask_b32_e64 v71, v155, v158, s[14:15]
	v_cndmask_b32_e64 v73, v156, v159, s[16:17]
	s_cmpk_gt_u32 s24, 0x9bf
	s_cbranch_scc1 .LBB0_49
	v_add_u32_e32 v72, s60, v150
	s_waitcnt vmcnt(16)
	ds_read_b128 v[94:97], v72
	s_waitcnt vmcnt(15)
	ds_read_b128 v[102:105], v72 offset:38016
	s_waitcnt vmcnt(14) lgkmcnt(1)
	v_mfma_f32_16x16x32_f16 v[46:49], v[94:97], v[98:101], v[46:49]
	s_waitcnt vmcnt(13)
	v_mfma_f32_16x16x32_f16 v[42:45], v[94:97], v[106:109], v[42:45]
	s_waitcnt vmcnt(12)
	v_mfma_f32_16x16x32_f16 v[34:37], v[94:97], v[110:113], v[34:37]
	ds_read_b128 v[94:97], v72 offset:12672
	ds_read_b128 v[122:125], v72 offset:25344
	s_waitcnt lgkmcnt(1)
	v_mfma_f32_16x16x32_f16 v[38:41], v[94:97], v[98:101], v[38:41]
	v_mfma_f32_16x16x32_f16 v[30:33], v[94:97], v[106:109], v[30:33]
	v_mfma_f32_16x16x32_f16 v[26:29], v[94:97], v[110:113], v[26:29]
	s_waitcnt lgkmcnt(0)
	v_mfma_f32_16x16x32_f16 v[22:25], v[122:125], v[98:101], v[22:25]
	v_mfma_f32_16x16x32_f16 v[18:21], v[122:125], v[106:109], v[18:21]
	v_mfma_f32_16x16x32_f16 v[14:17], v[122:125], v[110:113], v[14:17]
	v_mfma_f32_16x16x32_f16 v[10:13], v[102:105], v[98:101], v[10:13]
	v_mfma_f32_16x16x32_f16 v[6:9], v[102:105], v[106:109], v[6:9]
	v_mfma_f32_16x16x32_f16 v[2:5], v[102:105], v[110:113], v[2:5]
.LBB0_49:
	v_cndmask_b32_e64 v72, v70, v151, s[6:7]
	v_cndmask_b32_e64 v71, v71, v152, s[8:9]
	v_cndmask_b32_e64 v70, v73, v153, s[10:11]
	s_cmpk_gt_u32 s24, 0x7bf
	s_cbranch_scc1 .LBB0_51
	v_add_u32_e32 v73, s61, v150
	s_waitcnt vmcnt(16)
	ds_read_b128 v[94:97], v73
	s_waitcnt vmcnt(14)
	ds_read_b128 v[98:101], v73 offset:38016
	s_waitcnt vmcnt(11) lgkmcnt(1)
	v_mfma_f32_16x16x32_f16 v[46:49], v[94:97], v[86:89], v[46:49]
	s_waitcnt vmcnt(10)
	v_mfma_f32_16x16x32_f16 v[42:45], v[94:97], v[90:93], v[42:45]
	s_waitcnt vmcnt(9)
	v_mfma_f32_16x16x32_f16 v[34:37], v[94:97], v[114:117], v[34:37]
	ds_read_b128 v[94:97], v73 offset:12672
	ds_read_b128 v[102:105], v73 offset:25344
	s_waitcnt lgkmcnt(1)
	v_mfma_f32_16x16x32_f16 v[38:41], v[94:97], v[86:89], v[38:41]
	v_mfma_f32_16x16x32_f16 v[30:33], v[94:97], v[90:93], v[30:33]
	v_mfma_f32_16x16x32_f16 v[26:29], v[94:97], v[114:117], v[26:29]
	s_waitcnt lgkmcnt(0)
	v_mfma_f32_16x16x32_f16 v[22:25], v[102:105], v[86:89], v[22:25]
	v_mfma_f32_16x16x32_f16 v[18:21], v[102:105], v[90:93], v[18:21]
	v_mfma_f32_16x16x32_f16 v[14:17], v[102:105], v[114:117], v[14:17]
	v_mfma_f32_16x16x32_f16 v[10:13], v[98:101], v[86:89], v[10:13]
	v_mfma_f32_16x16x32_f16 v[6:9], v[98:101], v[90:93], v[6:9]
	v_mfma_f32_16x16x32_f16 v[2:5], v[98:101], v[114:117], v[2:5]
.LBB0_51:
	s_waitcnt vmcnt(11)
	v_mul_f32_e32 v87, 0x37800000, v72
	v_mov_b32_e32 v73, 0x260
	v_mul_f32_e32 v88, 0x37800000, v71
	v_mul_f32_e32 v86, 0x37800000, v70
	s_cmpk_gt_u32 s24, 0x5bf
	s_cbranch_scc1 .LBB0_53
	v_add_u32_e32 v89, s62, v150
	s_waitcnt vmcnt(10)
	ds_read_b128 v[90:93], v89
	ds_read_b128 v[94:97], v89 offset:38016
	s_waitcnt vmcnt(8) lgkmcnt(1)
	v_mfma_f32_16x16x32_f16 v[46:49], v[90:93], v[74:77], v[46:49]
	s_waitcnt vmcnt(7)
	v_mfma_f32_16x16x32_f16 v[42:45], v[90:93], v[78:81], v[42:45]
	s_waitcnt vmcnt(6)
	v_mfma_f32_16x16x32_f16 v[34:37], v[90:93], v[82:85], v[34:37]
	ds_read_b128 v[90:93], v89 offset:12672
	ds_read_b128 v[98:101], v89 offset:25344
	s_waitcnt lgkmcnt(1)
	v_mfma_f32_16x16x32_f16 v[38:41], v[90:93], v[74:77], v[38:41]
	v_mfma_f32_16x16x32_f16 v[30:33], v[90:93], v[78:81], v[30:33]
	v_mfma_f32_16x16x32_f16 v[26:29], v[90:93], v[82:85], v[26:29]
	s_waitcnt lgkmcnt(0)
	v_mfma_f32_16x16x32_f16 v[22:25], v[98:101], v[74:77], v[22:25]
	v_mfma_f32_16x16x32_f16 v[18:21], v[98:101], v[78:81], v[18:21]
	v_mfma_f32_16x16x32_f16 v[14:17], v[98:101], v[82:85], v[14:17]
	v_mfma_f32_16x16x32_f16 v[10:13], v[94:97], v[74:77], v[10:13]
	v_mfma_f32_16x16x32_f16 v[6:9], v[94:97], v[78:81], v[6:9]
	v_mfma_f32_16x16x32_f16 v[2:5], v[94:97], v[82:85], v[2:5]
.LBB0_53:
	v_cndmask_b32_e32 v72, v72, v87, vcc
	v_cmp_class_f32_e32 vcc, v147, v73
	v_cndmask_b32_e64 v71, v71, v88, s[2:3]
	v_cmp_class_f32_e64 s[2:3], v148, v73
	v_cndmask_b32_e64 v70, v70, v86, s[4:5]
	v_cmp_class_f32_e64 s[4:5], v149, v73
	s_cmpk_gt_u32 s24, 0x3bf
	s_cbranch_scc1 .LBB0_55
	v_add_u32_e32 v73, s63, v150
	s_waitcnt vmcnt(8)
	ds_read_b128 v[74:77], v73
	s_waitcnt vmcnt(7)
	ds_read_b128 v[78:81], v73 offset:38016
	s_waitcnt vmcnt(5) lgkmcnt(1)
	v_mfma_f32_16x16x32_f16 v[46:49], v[74:77], v[62:65], v[46:49]
	s_waitcnt vmcnt(4)
	v_mfma_f32_16x16x32_f16 v[42:45], v[74:77], v[66:69], v[42:45]
	s_waitcnt vmcnt(3)
	v_mfma_f32_16x16x32_f16 v[34:37], v[74:77], v[118:121], v[34:37]
	ds_read_b128 v[74:77], v73 offset:12672
	ds_read_b128 v[82:85], v73 offset:25344
	s_waitcnt lgkmcnt(1)
	v_mfma_f32_16x16x32_f16 v[38:41], v[74:77], v[62:65], v[38:41]
	v_mfma_f32_16x16x32_f16 v[30:33], v[74:77], v[66:69], v[30:33]
	v_mfma_f32_16x16x32_f16 v[26:29], v[74:77], v[118:121], v[26:29]
	s_waitcnt lgkmcnt(0)
	v_mfma_f32_16x16x32_f16 v[22:25], v[82:85], v[62:65], v[22:25]
	v_mfma_f32_16x16x32_f16 v[18:21], v[82:85], v[66:69], v[18:21]
	v_mfma_f32_16x16x32_f16 v[14:17], v[82:85], v[118:121], v[14:17]
	v_mfma_f32_16x16x32_f16 v[10:13], v[78:81], v[62:65], v[10:13]
	v_mfma_f32_16x16x32_f16 v[6:9], v[78:81], v[66:69], v[6:9]
	v_mfma_f32_16x16x32_f16 v[2:5], v[78:81], v[118:121], v[2:5]
.LBB0_55:
	s_load_dwordx2 s[6:7], s[0:1], 0x38
	s_waitcnt vmcnt(5)
	v_cndmask_b32_e32 v64, v72, v147, vcc
	v_cndmask_b32_e64 v63, v71, v148, s[2:3]
	v_cndmask_b32_e64 v62, v70, v149, s[4:5]
	s_cmpk_gt_u32 s24, 0x1bf
	s_cbranch_scc1 .LBB0_57
	v_add_u32_e32 v65, s64, v150
	s_waitcnt vmcnt(4)
	ds_read_b128 v[66:69], v65
	ds_read_b128 v[70:73], v65 offset:38016
	s_waitcnt vmcnt(2) lgkmcnt(0)
	v_mfma_f32_16x16x32_f16 v[46:49], v[66:69], v[50:53], v[46:49]
	s_waitcnt vmcnt(1)
	v_mfma_f32_16x16x32_f16 v[42:45], v[66:69], v[54:57], v[42:45]
	s_waitcnt vmcnt(0)
	v_mfma_f32_16x16x32_f16 v[34:37], v[66:69], v[58:61], v[34:37]
	ds_read_b128 v[66:69], v65 offset:12672
	ds_read_b128 v[74:77], v65 offset:25344
	s_waitcnt lgkmcnt(1)
	v_mfma_f32_16x16x32_f16 v[38:41], v[66:69], v[50:53], v[38:41]
	v_mfma_f32_16x16x32_f16 v[30:33], v[66:69], v[54:57], v[30:33]
	v_mfma_f32_16x16x32_f16 v[26:29], v[66:69], v[58:61], v[26:29]
	s_waitcnt lgkmcnt(0)
	v_mfma_f32_16x16x32_f16 v[22:25], v[74:77], v[50:53], v[22:25]
	v_mfma_f32_16x16x32_f16 v[18:21], v[74:77], v[54:57], v[18:21]
	v_mfma_f32_16x16x32_f16 v[14:17], v[74:77], v[58:61], v[14:17]
	v_mfma_f32_16x16x32_f16 v[10:13], v[70:73], v[50:53], v[10:13]
	v_mfma_f32_16x16x32_f16 v[6:9], v[70:73], v[54:57], v[6:9]
	v_mfma_f32_16x16x32_f16 v[2:5], v[70:73], v[58:61], v[2:5]
